# baseline (speedup 1.0000x reference)
.LBB1_128:
	s_lshl_b32 s1, s79, 8
	s_and_b32 s24, s1, 0x300
	s_ashr_i32 s1, s0, 31
	s_lshl_b64 s[4:5], s[0:1], 24
	s_add_u32 s26, s20, s4
	s_addc_u32 s27, s21, s5
	s_or_b32 s20, s24, s54
	v_or_b32_e32 v139, s20, v170
	v_lshlrev_b32_e32 v150, 1, v139
	v_lshlrev_b32_e32 v139, 7, v139
	v_lshl_add_u64 v[148:149], s[26:27], 0, v[150:151]
	v_and_b32_e32 v150, 0x1c00, v139
	s_cmp_lt_u32 s79, 4
	v_lshl_add_u64 v[140:141], s[26:27], 0, v[150:151]
	v_lshlrev_b32_e32 v150, 1, v142
	s_waitcnt vmcnt(0)
	v_pk_mul_f32 v[142:143], v[130:131], v[134:135] op_sel:[1,1] op_sel_hi:[1,0]
	v_mov_b32_e32 v138, s33
	s_cselect_b64 vcc, -1, 0
	v_pk_fma_f32 v[154:155], v[130:131], v[134:135], v[142:143] neg_lo:[0,0,1] neg_hi:[0,0,1]
	v_pk_fma_f32 v[130:131], v[130:131], v[134:135], v[142:143] op_sel_hi:[0,1,1]
	v_mov_b32_e32 v142, v133
	v_cndmask_b32_e32 v138, 1.0, v138, vcc
	v_mov_b32_e32 v155, v131
	v_pk_mul_f32 v[142:143], v[142:143], v[136:137] op_sel:[0,1] op_sel_hi:[0,0]
	v_pk_mul_f32 v[130:131], v[138:139], v[154:155] op_sel_hi:[0,1]
	v_pk_fma_f32 v[154:155], v[132:133], v[136:137], v[142:143] neg_lo:[0,0,1] neg_hi:[0,0,1]
	v_pk_fma_f32 v[132:133], v[132:133], v[136:137], v[142:143] op_sel_hi:[0,1,1]
	v_mov_b32_e32 v155, v133
	v_pk_mul_f32 v[142:143], v[126:127], v[66:67] op_sel:[1,1] op_sel_hi:[1,0]
	v_pk_mul_f32 v[132:133], v[138:139], v[154:155] op_sel_hi:[0,1]
	v_pk_fma_f32 v[154:155], v[126:127], v[66:67], v[142:143] neg_lo:[0,0,1] neg_hi:[0,0,1]
	v_pk_fma_f32 v[126:127], v[126:127], v[66:67], v[142:143] op_sel_hi:[0,1,1]
	v_mov_b32_e32 v126, v129
	v_mov_b32_e32 v155, v127
	v_pk_mul_f32 v[126:127], v[126:127], v[68:69] op_sel:[0,1] op_sel_hi:[0,0]
	v_pk_mul_f32 v[142:143], v[138:139], v[154:155] op_sel_hi:[0,1]
	v_pk_fma_f32 v[154:155], v[128:129], v[68:69], v[126:127] neg_lo:[0,0,1] neg_hi:[0,0,1]
	v_pk_fma_f32 v[126:127], v[128:129], v[68:69], v[126:127] op_sel_hi:[0,1,1]
	s_cmp_lg_u32 s0, 1
	v_ashrrev_i32_e32 v147, 31, v146
	v_mov_b32_e32 v155, v127
	s_cselect_b64 s[4:5], -1, 0
	v_lshlrev_b64 v[152:153], 11, v[146:147]
	v_pk_mul_f32 v[154:155], v[138:139], v[154:155] op_sel_hi:[0,1]
	s_ashr_i32 s21, s25, 7
	v_lshl_add_u64 v[152:153], v[148:149], 0, v[152:153]
	v_cvt_pk_f16_f32 v126, v130, v131
	v_cvt_pk_f16_f32 v127, v132, v133
	v_cvt_pk_f16_f32 v128, v142, v143
	v_cvt_pk_f16_f32 v129, v154, v155
	s_mov_b64 s[0:1], -1
	s_and_b64 vcc, exec, s[4:5]
	s_cbranch_vccz .LBB1_130
	v_mov_b64_e32 v[180:181], v[126:127]
	v_mov_b64_e32 v[182:183], v[128:129]
	v_mov_b64_e32 v[164:165], v[152:153]
	v_mov_b64_e32 v[166:167], v[152:153]
	s_mov_b32 s86, 0x40000
	s_mov_b32 s87, 0x8000
	s_mov_b32 s88, 0x100
	s_mov_b64 s[0:1], 0
.LBB1_130:
	s_and_b32 s24, s21, -16
	s_bfe_u32 s21, s25, 0x50006
	v_lshl_add_u64 v[130:131], v[140:141], 0, v[150:151]
	v_pk_mov_b32 v[154:155], v[134:135], v[134:135] op_sel:[1,0]
	v_mov_b32_e32 v139, v138
	v_pk_mov_b32 v[150:151], v[136:137], v[136:137] op_sel:[1,0]
	v_pk_mov_b32 v[142:143], v[66:67], v[66:67] op_sel:[1,0]
	s_andn2_b64 vcc, exec, s[0:1]
	v_pk_mov_b32 v[132:133], v[68:69], v[68:69] op_sel:[1,0]
	s_cbranch_vccnz .LBB1_132
	s_lshr_b32 s0, s20, 6
	s_or_b32 s0, s24, s0
	s_lshl_b32 s0, s0, 5
	s_or_b32 s0, s0, s21
	s_ashr_i32 s1, s0, 31
	s_lshl_b64 s[0:1], s[0:1], 13
	v_lshl_add_u64 v[156:157], v[130:131], 0, s[0:1]
	v_mov_b64_e32 v[180:181], v[126:127]
	v_mov_b64_e32 v[182:183], v[128:129]
	v_mov_b64_e32 v[164:165], v[156:157]
	v_mov_b64_e32 v[166:167], v[156:157]
	s_mov_b32 s86, 0x4000
	s_mov_b32 s87, 0x100
	s_mov_b32 s88, 0x80000
.LBB1_132:
	s_nop 1
	v_pk_mul_f32 v[126:127], v[122:123], v[154:155] op_sel:[1,0]
	s_andn2_b64 vcc, exec, s[4:5]
	v_pk_fma_f32 v[128:129], v[122:123], v[134:135], v[126:127] neg_lo:[0,0,1] neg_hi:[0,0,1]
	v_pk_fma_f32 v[122:123], v[122:123], v[134:135], v[126:127] op_sel_hi:[0,1,1]
	v_mov_b32_e32 v126, v125
	v_mov_b32_e32 v129, v123
	v_pk_mul_f32 v[126:127], v[126:127], v[150:151] op_sel_hi:[0,1]
	v_pk_mul_f32 v[122:123], v[138:139], v[128:129]
	v_pk_fma_f32 v[128:129], v[124:125], v[136:137], v[126:127] neg_lo:[0,0,1] neg_hi:[0,0,1]
	v_pk_fma_f32 v[124:125], v[124:125], v[136:137], v[126:127] op_sel_hi:[0,1,1]
	v_mov_b32_e32 v129, v125
	v_pk_mul_f32 v[126:127], v[118:119], v[142:143] op_sel:[1,0]
	v_pk_mul_f32 v[124:125], v[138:139], v[128:129]
	v_pk_fma_f32 v[128:129], v[118:119], v[66:67], v[126:127] neg_lo:[0,0,1] neg_hi:[0,0,1]
	v_pk_fma_f32 v[66:67], v[118:119], v[66:67], v[126:127] op_sel_hi:[0,1,1]
	v_mov_b32_e32 v66, v121
	v_mov_b32_e32 v129, v67
	v_pk_mul_f32 v[66:67], v[66:67], v[132:133] op_sel_hi:[0,1]
	v_pk_fma_f32 v[126:127], v[120:121], v[68:69], v[66:67] neg_lo:[0,0,1] neg_hi:[0,0,1]
	v_pk_fma_f32 v[66:67], v[120:121], v[68:69], v[66:67] op_sel_hi:[0,1,1]
	v_pk_mul_f32 v[118:119], v[138:139], v[128:129]
	v_mov_b32_e32 v127, v67
	v_pk_mul_f32 v[120:121], v[138:139], v[126:127]
	v_cvt_pk_f16_f32 v68, v118, v119
	v_cndmask_b32_e64 v118, 0, 1, s[4:5]
	v_cvt_pk_f16_f32 v66, v122, v123
	v_cvt_pk_f16_f32 v67, v124, v125
	v_cvt_pk_f16_f32 v69, v120, v121
	v_cmp_ne_u32_e64 s[0:1], 1, v118
	s_mov_b64 s[4:5], -1
	s_cbranch_vccnz .LBB1_134
	s_mov_b64 s[4:5], 0
	v_mov_b64_e32 v[184:185], v[66:67]
	v_mov_b64_e32 v[186:187], v[68:69]
.LBB1_134:
	s_andn2_b64 vcc, exec, s[4:5]
	s_cbranch_vccnz .LBB1_136
	s_lshr_b32 s4, s20, 6
	s_or_b32 s4, s24, s4
	s_lshl_b32 s4, s4, 5
	s_or_b32 s4, s21, s4
	s_or_b32 s4, s4, 64
	s_ashr_i32 s5, s4, 31
	s_lshl_b64 s[4:5], s[4:5], 13
	v_lshl_add_u64 v[118:119], v[130:131], 0, s[4:5]
	v_mov_b64_e32 v[184:185], v[66:67]
	v_mov_b64_e32 v[186:187], v[68:69]

.LBB1_138:
	v_ashrrev_i32_e32 v127, 31, v126
	v_lshlrev_b64 v[122:123], 11, v[126:127]
	v_lshlrev_b32_e32 v124, 4, v126
	s_waitcnt vmcnt(0)
	v_pk_mul_f32 v[126:127], v[114:115], v[118:119] op_sel:[1,1] op_sel_hi:[1,0]
	v_lshl_add_u64 v[122:123], v[148:149], 0, v[122:123]
	v_pk_fma_f32 v[128:129], v[114:115], v[118:119], v[126:127] neg_lo:[0,0,1] neg_hi:[0,0,1]
	v_pk_fma_f32 v[114:115], v[114:115], v[118:119], v[126:127] op_sel_hi:[0,1,1]
	v_mov_b32_e32 v126, v117
	v_mov_b32_e32 v129, v115
	v_pk_mul_f32 v[126:127], v[126:127], v[120:121] op_sel:[0,1] op_sel_hi:[0,0]
	v_pk_mul_f32 v[114:115], v[138:139], v[128:129]
	v_pk_fma_f32 v[128:129], v[116:117], v[120:121], v[126:127] neg_lo:[0,0,1] neg_hi:[0,0,1]
	v_pk_fma_f32 v[116:117], v[116:117], v[120:121], v[126:127] op_sel_hi:[0,1,1]
	v_mov_b32_e32 v129, v117
	v_pk_mul_f32 v[126:127], v[110:111], v[66:67] op_sel:[1,1] op_sel_hi:[1,0]
	v_pk_mul_f32 v[116:117], v[138:139], v[128:129]
	v_pk_fma_f32 v[128:129], v[110:111], v[66:67], v[126:127] neg_lo:[0,0,1] neg_hi:[0,0,1]
	v_pk_fma_f32 v[110:111], v[110:111], v[66:67], v[126:127] op_sel_hi:[0,1,1]
	v_mov_b32_e32 v110, v113
	v_mov_b32_e32 v129, v111
	v_pk_mul_f32 v[110:111], v[110:111], v[68:69] op_sel:[0,1] op_sel_hi:[0,0]
	v_pk_mul_f32 v[126:127], v[138:139], v[128:129]
	v_pk_fma_f32 v[128:129], v[112:113], v[68:69], v[110:111] neg_lo:[0,0,1] neg_hi:[0,0,1]
	v_pk_fma_f32 v[110:111], v[112:113], v[68:69], v[110:111] op_sel_hi:[0,1,1]
	v_mov_b32_e32 v129, v111
	v_pk_mul_f32 v[128:129], v[138:139], v[128:129]
	v_and_b32_e32 v124, 0x1f0, v124
	v_cvt_pk_f16_f32 v110, v114, v115
	v_cvt_pk_f16_f32 v111, v116, v117
	v_cvt_pk_f16_f32 v112, v126, v127
	v_cvt_pk_f16_f32 v113, v128, v129
	s_and_b64 vcc, exec, s[0:1]
	s_mov_b64 s[6:7], -1
	s_cbranch_vccnz .LBB1_140
	s_mov_b64 s[6:7], 0
	v_mov_b64_e32 v[188:189], v[110:111]
	v_mov_b64_e32 v[190:191], v[112:113]
.LBB1_140:
	v_lshl_add_u64 v[114:115], v[140:141], 0, v[124:125]
	v_pk_mov_b32 v[128:129], v[118:119], v[118:119] op_sel:[1,0]
	v_pk_mov_b32 v[126:127], v[120:121], v[120:121] op_sel:[1,0]
	v_pk_mov_b32 v[124:125], v[66:67], v[66:67] op_sel:[1,0]
	s_andn2_b64 vcc, exec, s[6:7]
	v_pk_mov_b32 v[116:117], v[68:69], v[68:69] op_sel:[1,0]
	s_cbranch_vccnz .LBB1_142
	s_lshr_b32 s6, s20, 6
	s_or_b32 s6, s24, s6
	s_lshl_b32 s6, s6, 5
	s_or_b32 s6, s6, s21
	s_ashr_i32 s7, s6, 31
	s_lshl_b64 s[6:7], s[6:7], 13
	v_lshl_add_u64 v[132:133], v[114:115], 0, s[6:7]
	v_mov_b64_e32 v[188:189], v[110:111]
	v_mov_b64_e32 v[190:191], v[112:113]
.LBB1_142:
	s_nop 1
	v_pk_mul_f32 v[110:111], v[106:107], v[128:129] op_sel:[1,0]
	s_and_b64 vcc, exec, s[0:1]
	v_pk_fma_f32 v[112:113], v[106:107], v[118:119], v[110:111] neg_lo:[0,0,1] neg_hi:[0,0,1]
	v_pk_fma_f32 v[106:107], v[106:107], v[118:119], v[110:111] op_sel_hi:[0,1,1]
	v_mov_b32_e32 v110, v109
	v_mov_b32_e32 v113, v107
	v_pk_mul_f32 v[110:111], v[110:111], v[126:127] op_sel_hi:[0,1]
	v_pk_mul_f32 v[106:107], v[138:139], v[112:113]
	v_pk_fma_f32 v[112:113], v[108:109], v[120:121], v[110:111] neg_lo:[0,0,1] neg_hi:[0,0,1]
	v_pk_fma_f32 v[108:109], v[108:109], v[120:121], v[110:111] op_sel_hi:[0,1,1]
	v_mov_b32_e32 v113, v109
	v_pk_mul_f32 v[110:111], v[102:103], v[124:125] op_sel:[1,0]
	v_pk_mul_f32 v[108:109], v[138:139], v[112:113]
	v_pk_fma_f32 v[112:113], v[102:103], v[66:67], v[110:111] neg_lo:[0,0,1] neg_hi:[0,0,1]
	v_pk_fma_f32 v[66:67], v[102:103], v[66:67], v[110:111] op_sel_hi:[0,1,1]
	v_mov_b32_e32 v66, v105
	v_mov_b32_e32 v113, v67
	v_pk_mul_f32 v[66:67], v[66:67], v[116:117] op_sel_hi:[0,1]
	v_pk_fma_f32 v[110:111], v[104:105], v[68:69], v[66:67] neg_lo:[0,0,1] neg_hi:[0,0,1]
	v_pk_fma_f32 v[66:67], v[104:105], v[68:69], v[66:67] op_sel_hi:[0,1,1]
	v_mov_b32_e32 v111, v67
	v_pk_mul_f32 v[102:103], v[138:139], v[112:113]
	v_pk_mul_f32 v[104:105], v[138:139], v[110:111]
	v_cvt_pk_f16_f32 v66, v106, v107
	v_cvt_pk_f16_f32 v67, v108, v109
	v_cvt_pk_f16_f32 v68, v102, v103
	v_cvt_pk_f16_f32 v69, v104, v105
	s_mov_b64 s[6:7], -1
	s_cbranch_vccnz .LBB1_144
	s_mov_b64 s[6:7], 0
	v_mov_b64_e32 v[192:193], v[66:67]
	v_mov_b64_e32 v[194:195], v[68:69]
.LBB1_144:
	s_andn2_b64 vcc, exec, s[6:7]
	s_cbranch_vccnz .LBB1_146
	s_lshr_b32 s6, s20, 6
	s_or_b32 s6, s24, s6
	s_lshl_b32 s6, s6, 5
	s_or_b32 s6, s21, s6
	s_or_b32 s6, s6, 64
	s_ashr_i32 s7, s6, 31
	s_lshl_b64 s[6:7], s[6:7], 13
	v_lshl_add_u64 v[102:103], v[114:115], 0, s[6:7]
	v_mov_b64_e32 v[192:193], v[66:67]
	v_mov_b64_e32 v[194:195], v[68:69]

.LBB1_148:
	v_ashrrev_i32_e32 v111, 31, v110
	v_lshlrev_b64 v[106:107], 11, v[110:111]
	v_lshlrev_b32_e32 v108, 4, v110
	s_waitcnt vmcnt(0)
	v_pk_mul_f32 v[110:111], v[98:99], v[102:103] op_sel:[1,1] op_sel_hi:[1,0]
	v_lshl_add_u64 v[106:107], v[148:149], 0, v[106:107]
	v_pk_fma_f32 v[112:113], v[98:99], v[102:103], v[110:111] neg_lo:[0,0,1] neg_hi:[0,0,1]
	v_pk_fma_f32 v[98:99], v[98:99], v[102:103], v[110:111] op_sel_hi:[0,1,1]
	v_mov_b32_e32 v110, v101
	v_mov_b32_e32 v113, v99
	v_pk_mul_f32 v[110:111], v[110:111], v[104:105] op_sel:[0,1] op_sel_hi:[0,0]
	v_pk_mul_f32 v[98:99], v[138:139], v[112:113]
	v_pk_fma_f32 v[112:113], v[100:101], v[104:105], v[110:111] neg_lo:[0,0,1] neg_hi:[0,0,1]
	v_pk_fma_f32 v[100:101], v[100:101], v[104:105], v[110:111] op_sel_hi:[0,1,1]
	v_mov_b32_e32 v113, v101
	v_pk_mul_f32 v[110:111], v[94:95], v[66:67] op_sel:[1,1] op_sel_hi:[1,0]
	v_pk_mul_f32 v[100:101], v[138:139], v[112:113]
	v_pk_fma_f32 v[112:113], v[94:95], v[66:67], v[110:111] neg_lo:[0,0,1] neg_hi:[0,0,1]
	v_pk_fma_f32 v[94:95], v[94:95], v[66:67], v[110:111] op_sel_hi:[0,1,1]
	v_mov_b32_e32 v94, v97
	v_mov_b32_e32 v113, v95
	v_pk_mul_f32 v[94:95], v[94:95], v[68:69] op_sel:[0,1] op_sel_hi:[0,0]
	v_pk_mul_f32 v[110:111], v[138:139], v[112:113]
	v_pk_fma_f32 v[112:113], v[96:97], v[68:69], v[94:95] neg_lo:[0,0,1] neg_hi:[0,0,1]
	v_pk_fma_f32 v[94:95], v[96:97], v[68:69], v[94:95] op_sel_hi:[0,1,1]
	v_mov_b32_e32 v113, v95
	v_pk_mul_f32 v[112:113], v[138:139], v[112:113]
	v_and_b32_e32 v108, 0x2f0, v108
	v_cvt_pk_f16_f32 v94, v98, v99
	v_cvt_pk_f16_f32 v95, v100, v101
	v_cvt_pk_f16_f32 v96, v110, v111
	v_cvt_pk_f16_f32 v97, v112, v113
	s_and_b64 vcc, exec, s[0:1]
	s_mov_b64 s[6:7], -1
	s_cbranch_vccnz .LBB1_150
	s_mov_b64 s[6:7], 0
	v_mov_b64_e32 v[196:197], v[94:95]
	v_mov_b64_e32 v[198:199], v[96:97]
.LBB1_150:
	v_lshl_add_u64 v[98:99], v[140:141], 0, v[108:109]
	v_pk_mov_b32 v[112:113], v[102:103], v[102:103] op_sel:[1,0]
	v_pk_mov_b32 v[110:111], v[104:105], v[104:105] op_sel:[1,0]
	v_pk_mov_b32 v[108:109], v[66:67], v[66:67] op_sel:[1,0]
	s_andn2_b64 vcc, exec, s[6:7]
	v_pk_mov_b32 v[100:101], v[68:69], v[68:69] op_sel:[1,0]
	s_cbranch_vccnz .LBB1_152
	s_lshr_b32 s6, s20, 6
	s_or_b32 s6, s24, s6
	s_lshl_b32 s6, s6, 5
	s_or_b32 s6, s6, s21
	s_ashr_i32 s7, s6, 31
	s_lshl_b64 s[6:7], s[6:7], 13
	v_lshl_add_u64 v[114:115], v[98:99], 0, s[6:7]
	v_mov_b64_e32 v[196:197], v[94:95]
	v_mov_b64_e32 v[198:199], v[96:97]
.LBB1_152:
	s_nop 1
	v_pk_mul_f32 v[94:95], v[90:91], v[112:113] op_sel:[1,0]
	s_and_b64 vcc, exec, s[0:1]
	v_pk_fma_f32 v[96:97], v[90:91], v[102:103], v[94:95] neg_lo:[0,0,1] neg_hi:[0,0,1]
	v_pk_fma_f32 v[90:91], v[90:91], v[102:103], v[94:95] op_sel_hi:[0,1,1]
	v_mov_b32_e32 v94, v93
	v_mov_b32_e32 v97, v91
	v_pk_mul_f32 v[94:95], v[94:95], v[110:111] op_sel_hi:[0,1]
	v_pk_mul_f32 v[90:91], v[138:139], v[96:97]
	v_pk_fma_f32 v[96:97], v[92:93], v[104:105], v[94:95] neg_lo:[0,0,1] neg_hi:[0,0,1]
	v_pk_fma_f32 v[92:93], v[92:93], v[104:105], v[94:95] op_sel_hi:[0,1,1]
	v_mov_b32_e32 v97, v93
	v_pk_mul_f32 v[94:95], v[86:87], v[108:109] op_sel:[1,0]
	v_pk_mul_f32 v[92:93], v[138:139], v[96:97]
	v_pk_fma_f32 v[96:97], v[86:87], v[66:67], v[94:95] neg_lo:[0,0,1] neg_hi:[0,0,1]
	v_pk_fma_f32 v[66:67], v[86:87], v[66:67], v[94:95] op_sel_hi:[0,1,1]
	v_mov_b32_e32 v66, v89
	v_mov_b32_e32 v97, v67
	v_pk_mul_f32 v[66:67], v[66:67], v[100:101] op_sel_hi:[0,1]
	v_pk_fma_f32 v[94:95], v[88:89], v[68:69], v[66:67] neg_lo:[0,0,1] neg_hi:[0,0,1]
	v_pk_fma_f32 v[66:67], v[88:89], v[68:69], v[66:67] op_sel_hi:[0,1,1]
	v_mov_b32_e32 v95, v67
	v_pk_mul_f32 v[86:87], v[138:139], v[96:97]
	v_pk_mul_f32 v[88:89], v[138:139], v[94:95]
	v_cvt_pk_f16_f32 v66, v90, v91
	v_cvt_pk_f16_f32 v67, v92, v93
	v_cvt_pk_f16_f32 v68, v86, v87
	v_cvt_pk_f16_f32 v69, v88, v89
	s_mov_b64 s[6:7], -1
	s_cbranch_vccnz .LBB1_154
	s_mov_b64 s[6:7], 0
	v_mov_b64_e32 v[200:201], v[66:67]
	v_mov_b64_e32 v[202:203], v[68:69]
.LBB1_154:
	s_andn2_b64 vcc, exec, s[6:7]
	s_cbranch_vccnz .LBB1_156
	s_lshr_b32 s6, s20, 6
	s_or_b32 s6, s24, s6
	s_lshl_b32 s6, s6, 5
	s_or_b32 s6, s21, s6
	s_or_b32 s6, s6, 64
	s_ashr_i32 s7, s6, 31
	s_lshl_b64 s[6:7], s[6:7], 13
	v_lshl_add_u64 v[86:87], v[98:99], 0, s[6:7]
	v_mov_b64_e32 v[200:201], v[66:67]
	v_mov_b64_e32 v[202:203], v[68:69]

.LBB1_158:
	v_ashrrev_i32_e32 v95, 31, v94
	v_lshlrev_b64 v[90:91], 11, v[94:95]
	v_lshlrev_b32_e32 v92, 4, v94
	s_waitcnt vmcnt(0)
	v_pk_mul_f32 v[94:95], v[82:83], v[86:87] op_sel:[1,1] op_sel_hi:[1,0]
	v_lshl_add_u64 v[90:91], v[148:149], 0, v[90:91]
	v_pk_fma_f32 v[96:97], v[82:83], v[86:87], v[94:95] neg_lo:[0,0,1] neg_hi:[0,0,1]
	v_pk_fma_f32 v[82:83], v[82:83], v[86:87], v[94:95] op_sel_hi:[0,1,1]
	v_mov_b32_e32 v94, v85
	v_mov_b32_e32 v97, v83
	v_pk_mul_f32 v[94:95], v[94:95], v[88:89] op_sel:[0,1] op_sel_hi:[0,0]
	v_pk_mul_f32 v[82:83], v[138:139], v[96:97]
	v_pk_fma_f32 v[96:97], v[84:85], v[88:89], v[94:95] neg_lo:[0,0,1] neg_hi:[0,0,1]
	v_pk_fma_f32 v[84:85], v[84:85], v[88:89], v[94:95] op_sel_hi:[0,1,1]
	v_mov_b32_e32 v97, v85
	v_pk_mul_f32 v[94:95], v[78:79], v[66:67] op_sel:[1,1] op_sel_hi:[1,0]
	v_pk_mul_f32 v[84:85], v[138:139], v[96:97]
	v_pk_fma_f32 v[96:97], v[78:79], v[66:67], v[94:95] neg_lo:[0,0,1] neg_hi:[0,0,1]
	v_pk_fma_f32 v[78:79], v[78:79], v[66:67], v[94:95] op_sel_hi:[0,1,1]
	v_mov_b32_e32 v78, v81
	v_mov_b32_e32 v97, v79
	v_pk_mul_f32 v[78:79], v[78:79], v[68:69] op_sel:[0,1] op_sel_hi:[0,0]
	v_pk_mul_f32 v[94:95], v[138:139], v[96:97]
	v_pk_fma_f32 v[96:97], v[80:81], v[68:69], v[78:79] neg_lo:[0,0,1] neg_hi:[0,0,1]
	v_pk_fma_f32 v[78:79], v[80:81], v[68:69], v[78:79] op_sel_hi:[0,1,1]
	v_mov_b32_e32 v97, v79
	v_pk_mul_f32 v[96:97], v[138:139], v[96:97]
	v_and_b32_e32 v92, 0x3f0, v92
	v_cvt_pk_f16_f32 v78, v82, v83
	v_cvt_pk_f16_f32 v79, v84, v85
	v_cvt_pk_f16_f32 v80, v94, v95
	v_cvt_pk_f16_f32 v81, v96, v97
	s_and_b64 vcc, exec, s[0:1]
	s_mov_b64 s[6:7], -1
	s_cbranch_vccnz .LBB1_160
	s_mov_b64 s[6:7], 0
	v_mov_b64_e32 v[204:205], v[78:79]
	v_mov_b64_e32 v[206:207], v[80:81]
.LBB1_160:
	v_lshl_add_u64 v[82:83], v[140:141], 0, v[92:93]
	v_pk_mov_b32 v[96:97], v[86:87], v[86:87] op_sel:[1,0]
	v_pk_mov_b32 v[94:95], v[88:89], v[88:89] op_sel:[1,0]
	v_pk_mov_b32 v[92:93], v[66:67], v[66:67] op_sel:[1,0]
	s_andn2_b64 vcc, exec, s[6:7]
	v_pk_mov_b32 v[84:85], v[68:69], v[68:69] op_sel:[1,0]
	s_cbranch_vccnz .LBB1_162
	s_lshr_b32 s6, s20, 6
	s_or_b32 s6, s24, s6
	s_lshl_b32 s6, s6, 5
	s_or_b32 s6, s6, s21
	s_ashr_i32 s7, s6, 31
	s_lshl_b64 s[6:7], s[6:7], 13
	v_lshl_add_u64 v[98:99], v[82:83], 0, s[6:7]
	v_mov_b64_e32 v[204:205], v[78:79]
	v_mov_b64_e32 v[206:207], v[80:81]

.LBB1_166:
	v_mov_b64_e32 v[208:209], v[66:67]
	v_mov_b64_e32 v[210:211], v[68:69]
	s_cbranch_execnz .LBB1_164
.LBB1_167:
	s_lshr_b32 s6, s20, 6
	s_or_b32 s6, s24, s6
	s_lshl_b32 s6, s6, 5
	s_or_b32 s6, s21, s6
	s_or_b32 s6, s6, 64
	s_ashr_i32 s7, s6, 31
	s_lshl_b64 s[6:7], s[6:7], 13
	v_lshl_add_u64 v[70:71], v[82:83], 0, s[6:7]
	v_mov_b64_e32 v[208:209], v[66:67]
	v_mov_b64_e32 v[210:211], v[68:69]
	s_and_b64 vcc, exec, s[4:5]
	v_add_u32_e32 v76, 0x80, v146
	s_cbranch_vccz .LBB1_165

.LBB1_169:
	s_waitcnt vmcnt(0)
	v_pk_mul_f32 v[80:81], v[62:63], v[70:71] op_sel:[1,1] op_sel_hi:[1,0]
	v_ashrrev_i32_e32 v77, 31, v76
	v_pk_fma_f32 v[82:83], v[62:63], v[70:71], v[80:81] neg_lo:[0,0,1] neg_hi:[0,0,1]
	v_pk_fma_f32 v[62:63], v[62:63], v[70:71], v[80:81] op_sel_hi:[0,1,1]
	v_mov_b32_e32 v80, v65
	v_mov_b32_e32 v83, v63
	v_pk_mul_f32 v[80:81], v[80:81], v[72:73] op_sel:[0,1] op_sel_hi:[0,0]
	v_pk_mul_f32 v[62:63], v[138:139], v[82:83]
	v_pk_fma_f32 v[82:83], v[64:65], v[72:73], v[80:81] neg_lo:[0,0,1] neg_hi:[0,0,1]
	v_pk_fma_f32 v[64:65], v[64:65], v[72:73], v[80:81] op_sel_hi:[0,1,1]
	v_mov_b32_e32 v83, v65
	v_pk_mul_f32 v[80:81], v[58:59], v[66:67] op_sel:[1,1] op_sel_hi:[1,0]
	v_pk_mul_f32 v[64:65], v[138:139], v[82:83]
	v_pk_fma_f32 v[82:83], v[58:59], v[66:67], v[80:81] neg_lo:[0,0,1] neg_hi:[0,0,1]
	v_pk_fma_f32 v[58:59], v[58:59], v[66:67], v[80:81] op_sel_hi:[0,1,1]
	v_mov_b32_e32 v58, v61
	v_mov_b32_e32 v83, v59
	v_pk_mul_f32 v[58:59], v[58:59], v[68:69] op_sel:[0,1] op_sel_hi:[0,0]
	v_pk_mul_f32 v[80:81], v[138:139], v[82:83]
	v_pk_fma_f32 v[82:83], v[60:61], v[68:69], v[58:59] neg_lo:[0,0,1] neg_hi:[0,0,1]
	v_pk_fma_f32 v[58:59], v[60:61], v[68:69], v[58:59] op_sel_hi:[0,1,1]
	v_mov_b32_e32 v83, v59
	v_lshlrev_b64 v[74:75], 11, v[76:77]
	v_pk_mul_f32 v[82:83], v[138:139], v[82:83]
	v_ashrrev_i32_e32 v78, 7, v76
	v_lshl_add_u64 v[74:75], v[148:149], 0, v[74:75]
	v_cvt_pk_f16_f32 v58, v62, v63
	v_cvt_pk_f16_f32 v59, v64, v65
	v_cvt_pk_f16_f32 v60, v80, v81
	v_cvt_pk_f16_f32 v61, v82, v83
	s_and_b64 vcc, exec, s[0:1]
	s_mov_b64 s[6:7], -1
	s_cbranch_vccnz .LBB1_171
	s_mov_b64 s[6:7], 0
	v_mov_b64_e32 v[212:213], v[58:59]
	v_mov_b64_e32 v[214:215], v[60:61]
.LBB1_171:
	v_and_b32_e32 v81, -16, v78
	v_bfe_u32 v80, v76, 6, 5
	v_pk_mov_b32 v[78:79], v[70:71], v[70:71] op_sel:[1,0]
	v_pk_mov_b32 v[76:77], v[72:73], v[72:73] op_sel:[1,0]
	v_pk_mov_b32 v[64:65], v[66:67], v[66:67] op_sel:[1,0]
	s_andn2_b64 vcc, exec, s[6:7]
	v_pk_mov_b32 v[62:63], v[68:69], v[68:69] op_sel:[1,0]
	s_cbranch_vccnz .LBB1_173
	s_lshr_b32 s6, s20, 6
	v_or_b32_e32 v82, s6, v81
	v_lshl_or_b32 v82, v82, 5, v80
	v_ashrrev_i32_e32 v83, 31, v82
	v_lshlrev_b64 v[82:83], 13, v[82:83]
	v_lshl_add_u64 v[82:83], v[130:131], 0, v[82:83]
	v_mov_b64_e32 v[212:213], v[58:59]
	v_mov_b64_e32 v[214:215], v[60:61]
.LBB1_173:
	s_nop 1
	v_pk_mul_f32 v[58:59], v[54:55], v[78:79] op_sel:[1,0]
	s_and_b64 vcc, exec, s[0:1]
	v_pk_fma_f32 v[60:61], v[54:55], v[70:71], v[58:59] neg_lo:[0,0,1] neg_hi:[0,0,1]
	v_pk_fma_f32 v[54:55], v[54:55], v[70:71], v[58:59] op_sel_hi:[0,1,1]
	v_mov_b32_e32 v58, v57
	v_mov_b32_e32 v61, v55
	v_pk_mul_f32 v[58:59], v[58:59], v[76:77] op_sel_hi:[0,1]
	v_pk_mul_f32 v[54:55], v[138:139], v[60:61]
	v_pk_fma_f32 v[60:61], v[56:57], v[72:73], v[58:59] neg_lo:[0,0,1] neg_hi:[0,0,1]
	v_pk_fma_f32 v[56:57], v[56:57], v[72:73], v[58:59] op_sel_hi:[0,1,1]
	v_mov_b32_e32 v61, v57
	v_pk_mul_f32 v[58:59], v[50:51], v[64:65] op_sel:[1,0]
	v_pk_mul_f32 v[56:57], v[138:139], v[60:61]
	v_pk_fma_f32 v[60:61], v[50:51], v[66:67], v[58:59] neg_lo:[0,0,1] neg_hi:[0,0,1]
	v_pk_fma_f32 v[50:51], v[50:51], v[66:67], v[58:59] op_sel_hi:[0,1,1]
	v_mov_b32_e32 v50, v53
	v_mov_b32_e32 v61, v51
	v_pk_mul_f32 v[50:51], v[50:51], v[62:63] op_sel_hi:[0,1]
	v_pk_mul_f32 v[58:59], v[138:139], v[60:61]
	v_pk_fma_f32 v[60:61], v[52:53], v[68:69], v[50:51] neg_lo:[0,0,1] neg_hi:[0,0,1]
	v_pk_fma_f32 v[50:51], v[52:53], v[68:69], v[50:51] op_sel_hi:[0,1,1]
	v_mov_b32_e32 v61, v51
	v_pk_mul_f32 v[60:61], v[138:139], v[60:61]
	v_cvt_pk_f16_f32 v50, v54, v55
	v_cvt_pk_f16_f32 v51, v56, v57
	v_cvt_pk_f16_f32 v52, v58, v59
	v_cvt_pk_f16_f32 v53, v60, v61
	s_mov_b64 s[6:7], -1
	s_cbranch_vccnz .LBB1_175
	s_mov_b64 s[6:7], 0
	v_mov_b64_e32 v[216:217], v[50:51]
	v_mov_b64_e32 v[218:219], v[52:53]
.LBB1_175:
	s_andn2_b64 vcc, exec, s[6:7]
	s_cbranch_vccnz .LBB1_177
	s_lshr_b32 s6, s20, 6
	v_or_b32_e32 v54, s6, v81
	v_lshlrev_b32_e32 v54, 5, v54
	v_or3_b32 v54, v80, v54, 64
	v_ashrrev_i32_e32 v55, 31, v54
	v_lshlrev_b64 v[54:55], 13, v[54:55]
	v_lshl_add_u64 v[54:55], v[130:131], 0, v[54:55]
	v_mov_b64_e32 v[216:217], v[50:51]
	v_mov_b64_e32 v[218:219], v[52:53]

.LBB1_179:
	v_ashrrev_i32_e32 v63, 31, v62
	v_lshlrev_b64 v[58:59], 11, v[62:63]
	v_lshlrev_b32_e32 v60, 4, v62
	s_waitcnt vmcnt(0)
	v_pk_mul_f32 v[62:63], v[46:47], v[54:55] op_sel:[1,1] op_sel_hi:[1,0]
	v_lshl_add_u64 v[58:59], v[148:149], 0, v[58:59]
	v_pk_fma_f32 v[64:65], v[46:47], v[54:55], v[62:63] neg_lo:[0,0,1] neg_hi:[0,0,1]
	v_pk_fma_f32 v[46:47], v[46:47], v[54:55], v[62:63] op_sel_hi:[0,1,1]
	v_mov_b32_e32 v62, v49
	v_mov_b32_e32 v65, v47
	v_pk_mul_f32 v[62:63], v[62:63], v[56:57] op_sel:[0,1] op_sel_hi:[0,0]
	v_pk_mul_f32 v[46:47], v[138:139], v[64:65]
	v_pk_fma_f32 v[64:65], v[48:49], v[56:57], v[62:63] neg_lo:[0,0,1] neg_hi:[0,0,1]
	v_pk_fma_f32 v[48:49], v[48:49], v[56:57], v[62:63] op_sel_hi:[0,1,1]
	v_mov_b32_e32 v65, v49
	v_pk_mul_f32 v[62:63], v[42:43], v[50:51] op_sel:[1,1] op_sel_hi:[1,0]
	v_pk_mul_f32 v[48:49], v[138:139], v[64:65]
	v_pk_fma_f32 v[64:65], v[42:43], v[50:51], v[62:63] neg_lo:[0,0,1] neg_hi:[0,0,1]
	v_pk_fma_f32 v[42:43], v[42:43], v[50:51], v[62:63] op_sel_hi:[0,1,1]
	v_mov_b32_e32 v42, v45
	v_mov_b32_e32 v65, v43
	v_pk_mul_f32 v[42:43], v[42:43], v[52:53] op_sel:[0,1] op_sel_hi:[0,0]
	v_pk_mul_f32 v[62:63], v[138:139], v[64:65]
	v_pk_fma_f32 v[64:65], v[44:45], v[52:53], v[42:43] neg_lo:[0,0,1] neg_hi:[0,0,1]
	v_pk_fma_f32 v[42:43], v[44:45], v[52:53], v[42:43] op_sel_hi:[0,1,1]
	v_mov_b32_e32 v65, v43
	v_pk_mul_f32 v[64:65], v[138:139], v[64:65]
	v_and_b32_e32 v60, 0x1f0, v60
	v_cvt_pk_f16_f32 v42, v46, v47
	v_cvt_pk_f16_f32 v43, v48, v49
	v_cvt_pk_f16_f32 v44, v62, v63
	v_cvt_pk_f16_f32 v45, v64, v65
	s_and_b64 vcc, exec, s[0:1]
	s_mov_b64 s[6:7], -1
	s_cbranch_vccnz .LBB1_181
	s_mov_b64 s[6:7], 0
	v_mov_b64_e32 v[220:221], v[42:43]
	v_mov_b64_e32 v[222:223], v[44:45]
.LBB1_181:
	v_lshl_add_u64 v[46:47], v[140:141], 0, v[60:61]
	v_pk_mov_b32 v[64:65], v[54:55], v[54:55] op_sel:[1,0]
	v_pk_mov_b32 v[62:63], v[56:57], v[56:57] op_sel:[1,0]
	v_pk_mov_b32 v[60:61], v[50:51], v[50:51] op_sel:[1,0]
	s_andn2_b64 vcc, exec, s[6:7]
	v_pk_mov_b32 v[48:49], v[52:53], v[52:53] op_sel:[1,0]
	s_cbranch_vccnz .LBB1_183
	s_lshr_b32 s6, s20, 6
	v_or_b32_e32 v66, s6, v81
	v_lshl_or_b32 v66, v66, 5, v80
	v_ashrrev_i32_e32 v67, 31, v66
	v_lshlrev_b64 v[66:67], 13, v[66:67]
	v_lshl_add_u64 v[66:67], v[46:47], 0, v[66:67]
	v_mov_b64_e32 v[220:221], v[42:43]
	v_mov_b64_e32 v[222:223], v[44:45]
.LBB1_183:
	s_nop 1
	v_pk_mul_f32 v[42:43], v[38:39], v[64:65] op_sel:[1,0]
	s_and_b64 vcc, exec, s[0:1]
	v_pk_fma_f32 v[44:45], v[38:39], v[54:55], v[42:43] neg_lo:[0,0,1] neg_hi:[0,0,1]
	v_pk_fma_f32 v[38:39], v[38:39], v[54:55], v[42:43] op_sel_hi:[0,1,1]
	v_mov_b32_e32 v42, v41
	v_mov_b32_e32 v45, v39
	v_pk_mul_f32 v[42:43], v[42:43], v[62:63] op_sel_hi:[0,1]
	v_pk_mul_f32 v[38:39], v[138:139], v[44:45]
	v_pk_fma_f32 v[44:45], v[40:41], v[56:57], v[42:43] neg_lo:[0,0,1] neg_hi:[0,0,1]
	v_pk_fma_f32 v[40:41], v[40:41], v[56:57], v[42:43] op_sel_hi:[0,1,1]
	v_mov_b32_e32 v45, v41
	v_pk_mul_f32 v[42:43], v[34:35], v[60:61] op_sel:[1,0]
	v_pk_mul_f32 v[40:41], v[138:139], v[44:45]
	v_pk_fma_f32 v[44:45], v[34:35], v[50:51], v[42:43] neg_lo:[0,0,1] neg_hi:[0,0,1]
	v_pk_fma_f32 v[34:35], v[34:35], v[50:51], v[42:43] op_sel_hi:[0,1,1]
	v_mov_b32_e32 v34, v37
	v_mov_b32_e32 v45, v35
	v_pk_mul_f32 v[34:35], v[34:35], v[48:49] op_sel_hi:[0,1]
	v_pk_mul_f32 v[42:43], v[138:139], v[44:45]
	v_pk_fma_f32 v[44:45], v[36:37], v[52:53], v[34:35] neg_lo:[0,0,1] neg_hi:[0,0,1]
	v_pk_fma_f32 v[34:35], v[36:37], v[52:53], v[34:35] op_sel_hi:[0,1,1]
	v_mov_b32_e32 v45, v35
	v_pk_mul_f32 v[44:45], v[138:139], v[44:45]
	v_cvt_pk_f16_f32 v34, v38, v39
	v_cvt_pk_f16_f32 v35, v40, v41
	v_cvt_pk_f16_f32 v36, v42, v43
	v_cvt_pk_f16_f32 v37, v44, v45
	s_mov_b64 s[6:7], -1
	s_cbranch_vccnz .LBB1_185
	s_mov_b64 s[6:7], 0
	v_mov_b64_e32 v[224:225], v[34:35]
	v_mov_b64_e32 v[226:227], v[36:37]
.LBB1_185:
	s_andn2_b64 vcc, exec, s[6:7]
	s_cbranch_vccnz .LBB1_187
	s_lshr_b32 s6, s20, 6
	v_or_b32_e32 v38, s6, v81
	v_lshlrev_b32_e32 v38, 5, v38
	v_or3_b32 v38, v80, v38, 64
	v_ashrrev_i32_e32 v39, 31, v38
	v_lshlrev_b64 v[38:39], 13, v[38:39]
	v_lshl_add_u64 v[38:39], v[46:47], 0, v[38:39]
	v_mov_b64_e32 v[224:225], v[34:35]
	v_mov_b64_e32 v[226:227], v[36:37]

.LBB1_189:
	v_ashrrev_i32_e32 v47, 31, v46
	v_lshlrev_b64 v[42:43], 11, v[46:47]
	v_lshlrev_b32_e32 v44, 4, v46
	s_waitcnt vmcnt(0)
	v_pk_mul_f32 v[46:47], v[30:31], v[38:39] op_sel:[1,1] op_sel_hi:[1,0]
	v_lshl_add_u64 v[42:43], v[148:149], 0, v[42:43]
	v_pk_fma_f32 v[48:49], v[30:31], v[38:39], v[46:47] neg_lo:[0,0,1] neg_hi:[0,0,1]
	v_pk_fma_f32 v[30:31], v[30:31], v[38:39], v[46:47] op_sel_hi:[0,1,1]
	v_mov_b32_e32 v46, v33
	v_mov_b32_e32 v49, v31
	v_pk_mul_f32 v[46:47], v[46:47], v[40:41] op_sel:[0,1] op_sel_hi:[0,0]
	v_pk_mul_f32 v[30:31], v[138:139], v[48:49]
	v_pk_fma_f32 v[48:49], v[32:33], v[40:41], v[46:47] neg_lo:[0,0,1] neg_hi:[0,0,1]
	v_pk_fma_f32 v[32:33], v[32:33], v[40:41], v[46:47] op_sel_hi:[0,1,1]
	v_mov_b32_e32 v49, v33
	v_pk_mul_f32 v[46:47], v[26:27], v[34:35] op_sel:[1,1] op_sel_hi:[1,0]
	v_pk_mul_f32 v[32:33], v[138:139], v[48:49]
	v_pk_fma_f32 v[48:49], v[26:27], v[34:35], v[46:47] neg_lo:[0,0,1] neg_hi:[0,0,1]
	v_pk_fma_f32 v[26:27], v[26:27], v[34:35], v[46:47] op_sel_hi:[0,1,1]
	v_mov_b32_e32 v26, v29
	v_mov_b32_e32 v49, v27
	v_pk_mul_f32 v[26:27], v[26:27], v[36:37] op_sel:[0,1] op_sel_hi:[0,0]
	v_pk_mul_f32 v[46:47], v[138:139], v[48:49]
	v_pk_fma_f32 v[48:49], v[28:29], v[36:37], v[26:27] neg_lo:[0,0,1] neg_hi:[0,0,1]
	v_pk_fma_f32 v[26:27], v[28:29], v[36:37], v[26:27] op_sel_hi:[0,1,1]
	v_mov_b32_e32 v49, v27
	v_pk_mul_f32 v[48:49], v[138:139], v[48:49]
	v_and_b32_e32 v44, 0x2f0, v44
	v_cvt_pk_f16_f32 v26, v30, v31
	v_cvt_pk_f16_f32 v27, v32, v33
	v_cvt_pk_f16_f32 v28, v46, v47
	v_cvt_pk_f16_f32 v29, v48, v49
	s_and_b64 vcc, exec, s[0:1]
	s_mov_b64 s[6:7], -1
	s_cbranch_vccnz .LBB1_191
	s_mov_b64 s[6:7], 0
	v_mov_b64_e32 v[228:229], v[26:27]
	v_mov_b64_e32 v[230:231], v[28:29]
.LBB1_191:
	v_lshl_add_u64 v[30:31], v[140:141], 0, v[44:45]
	v_pk_mov_b32 v[48:49], v[38:39], v[38:39] op_sel:[1,0]
	v_pk_mov_b32 v[46:47], v[40:41], v[40:41] op_sel:[1,0]
	v_pk_mov_b32 v[44:45], v[34:35], v[34:35] op_sel:[1,0]
	s_andn2_b64 vcc, exec, s[6:7]
	v_pk_mov_b32 v[32:33], v[36:37], v[36:37] op_sel:[1,0]
	s_cbranch_vccnz .LBB1_193
	s_lshr_b32 s6, s20, 6
	v_or_b32_e32 v50, s6, v81
	v_lshl_or_b32 v50, v50, 5, v80
	v_ashrrev_i32_e32 v51, 31, v50
	v_lshlrev_b64 v[50:51], 13, v[50:51]
	v_lshl_add_u64 v[50:51], v[30:31], 0, v[50:51]
	v_mov_b64_e32 v[228:229], v[26:27]
	v_mov_b64_e32 v[230:231], v[28:29]
.LBB1_193:
	s_nop 1
	v_pk_mul_f32 v[26:27], v[22:23], v[48:49] op_sel:[1,0]
	s_and_b64 vcc, exec, s[0:1]
	v_pk_fma_f32 v[28:29], v[22:23], v[38:39], v[26:27] neg_lo:[0,0,1] neg_hi:[0,0,1]
	v_pk_fma_f32 v[22:23], v[22:23], v[38:39], v[26:27] op_sel_hi:[0,1,1]
	v_mov_b32_e32 v26, v25
	v_mov_b32_e32 v29, v23
	v_pk_mul_f32 v[26:27], v[26:27], v[46:47] op_sel_hi:[0,1]
	v_pk_mul_f32 v[22:23], v[138:139], v[28:29]
	v_pk_fma_f32 v[28:29], v[24:25], v[40:41], v[26:27] neg_lo:[0,0,1] neg_hi:[0,0,1]
	v_pk_fma_f32 v[24:25], v[24:25], v[40:41], v[26:27] op_sel_hi:[0,1,1]
	v_mov_b32_e32 v29, v25
	v_pk_mul_f32 v[26:27], v[18:19], v[44:45] op_sel:[1,0]
	v_pk_mul_f32 v[24:25], v[138:139], v[28:29]
	v_pk_fma_f32 v[28:29], v[18:19], v[34:35], v[26:27] neg_lo:[0,0,1] neg_hi:[0,0,1]
	v_pk_fma_f32 v[18:19], v[18:19], v[34:35], v[26:27] op_sel_hi:[0,1,1]
	v_mov_b32_e32 v18, v21
	v_mov_b32_e32 v29, v19
	v_pk_mul_f32 v[18:19], v[18:19], v[32:33] op_sel_hi:[0,1]
	v_pk_mul_f32 v[26:27], v[138:139], v[28:29]
	v_pk_fma_f32 v[28:29], v[20:21], v[36:37], v[18:19] neg_lo:[0,0,1] neg_hi:[0,0,1]
	v_pk_fma_f32 v[18:19], v[20:21], v[36:37], v[18:19] op_sel_hi:[0,1,1]
	v_mov_b32_e32 v29, v19
	v_pk_mul_f32 v[28:29], v[138:139], v[28:29]
	v_cvt_pk_f16_f32 v18, v22, v23
	v_cvt_pk_f16_f32 v19, v24, v25
	v_cvt_pk_f16_f32 v20, v26, v27
	v_cvt_pk_f16_f32 v21, v28, v29
	s_mov_b64 s[6:7], -1
	s_cbranch_vccnz .LBB1_195
	s_mov_b64 s[6:7], 0
	v_mov_b64_e32 v[232:233], v[18:19]
	v_mov_b64_e32 v[234:235], v[20:21]
.LBB1_195:
	s_andn2_b64 vcc, exec, s[6:7]
	s_cbranch_vccnz .LBB1_197
	s_lshr_b32 s6, s20, 6
	v_or_b32_e32 v22, s6, v81
	v_lshlrev_b32_e32 v22, 5, v22
	v_or3_b32 v22, v80, v22, 64
	v_ashrrev_i32_e32 v23, 31, v22
	v_lshlrev_b64 v[22:23], 13, v[22:23]
	v_lshl_add_u64 v[22:23], v[30:31], 0, v[22:23]
	v_mov_b64_e32 v[232:233], v[18:19]
	v_mov_b64_e32 v[234:235], v[20:21]

.LBB1_199:
	v_ashrrev_i32_e32 v31, 31, v30
	v_lshlrev_b64 v[26:27], 11, v[30:31]
	v_lshlrev_b32_e32 v28, 4, v30
	s_waitcnt vmcnt(0)
	v_pk_mul_f32 v[30:31], v[14:15], v[22:23] op_sel:[1,1] op_sel_hi:[1,0]
	v_lshl_add_u64 v[26:27], v[148:149], 0, v[26:27]
	v_pk_fma_f32 v[32:33], v[14:15], v[22:23], v[30:31] neg_lo:[0,0,1] neg_hi:[0,0,1]
	v_pk_fma_f32 v[14:15], v[14:15], v[22:23], v[30:31] op_sel_hi:[0,1,1]
	v_mov_b32_e32 v30, v17
	v_mov_b32_e32 v33, v15
	v_pk_mul_f32 v[30:31], v[30:31], v[24:25] op_sel:[0,1] op_sel_hi:[0,0]
	v_pk_mul_f32 v[14:15], v[138:139], v[32:33]
	v_pk_fma_f32 v[32:33], v[16:17], v[24:25], v[30:31] neg_lo:[0,0,1] neg_hi:[0,0,1]
	v_pk_fma_f32 v[16:17], v[16:17], v[24:25], v[30:31] op_sel_hi:[0,1,1]
	v_mov_b32_e32 v33, v17
	v_pk_mul_f32 v[30:31], v[10:11], v[18:19] op_sel:[1,1] op_sel_hi:[1,0]
	v_pk_mul_f32 v[16:17], v[138:139], v[32:33]
	v_pk_fma_f32 v[32:33], v[10:11], v[18:19], v[30:31] neg_lo:[0,0,1] neg_hi:[0,0,1]
	v_pk_fma_f32 v[10:11], v[10:11], v[18:19], v[30:31] op_sel_hi:[0,1,1]
	v_mov_b32_e32 v10, v13
	v_mov_b32_e32 v33, v11
	v_pk_mul_f32 v[10:11], v[10:11], v[20:21] op_sel:[0,1] op_sel_hi:[0,0]
	v_pk_mul_f32 v[30:31], v[138:139], v[32:33]
	v_pk_fma_f32 v[32:33], v[12:13], v[20:21], v[10:11] neg_lo:[0,0,1] neg_hi:[0,0,1]
	v_pk_fma_f32 v[10:11], v[12:13], v[20:21], v[10:11] op_sel_hi:[0,1,1]
	v_mov_b32_e32 v33, v11
	v_pk_mul_f32 v[32:33], v[138:139], v[32:33]
	v_and_b32_e32 v28, 0x3f0, v28
	v_cvt_pk_f16_f32 v10, v14, v15
	v_cvt_pk_f16_f32 v11, v16, v17
	v_cvt_pk_f16_f32 v12, v30, v31
	v_cvt_pk_f16_f32 v13, v32, v33
	s_and_b64 vcc, exec, s[0:1]
	s_mov_b64 s[4:5], -1
	s_cbranch_vccnz .LBB1_201
	s_mov_b64 s[4:5], 0
	v_mov_b64_e32 v[236:237], v[10:11]
	v_mov_b64_e32 v[238:239], v[12:13]
.LBB1_201:
	v_lshl_add_u64 v[14:15], v[140:141], 0, v[28:29]
	v_pk_mov_b32 v[32:33], v[22:23], v[22:23] op_sel:[1,0]
	v_pk_mov_b32 v[30:31], v[24:25], v[24:25] op_sel:[1,0]
	v_pk_mov_b32 v[28:29], v[18:19], v[18:19] op_sel:[1,0]
	s_andn2_b64 vcc, exec, s[4:5]
	v_pk_mov_b32 v[16:17], v[20:21], v[20:21] op_sel:[1,0]
	s_cbranch_vccnz .LBB1_203
	s_lshr_b32 s4, s20, 6
	v_or_b32_e32 v34, s4, v81
	v_lshl_or_b32 v34, v34, 5, v80
	v_ashrrev_i32_e32 v35, 31, v34
	v_lshlrev_b64 v[34:35], 13, v[34:35]
	v_lshl_add_u64 v[34:35], v[14:15], 0, v[34:35]
	v_mov_b64_e32 v[236:237], v[10:11]
	v_mov_b64_e32 v[238:239], v[12:13]
.LBB1_203:
	s_nop 1
	v_pk_mul_f32 v[10:11], v[6:7], v[32:33] op_sel:[1,0]
	s_and_b64 vcc, exec, s[0:1]
	v_pk_fma_f32 v[12:13], v[6:7], v[22:23], v[10:11] neg_lo:[0,0,1] neg_hi:[0,0,1]
	v_pk_fma_f32 v[6:7], v[6:7], v[22:23], v[10:11] op_sel_hi:[0,1,1]
	v_mov_b32_e32 v10, v9
	v_mov_b32_e32 v13, v7
	v_pk_mul_f32 v[10:11], v[10:11], v[30:31] op_sel_hi:[0,1]
	v_pk_mul_f32 v[6:7], v[138:139], v[12:13]
	v_pk_fma_f32 v[12:13], v[8:9], v[24:25], v[10:11] neg_lo:[0,0,1] neg_hi:[0,0,1]
	v_pk_fma_f32 v[8:9], v[8:9], v[24:25], v[10:11] op_sel_hi:[0,1,1]
	v_mov_b32_e32 v13, v9
	v_pk_mul_f32 v[10:11], v[2:3], v[28:29] op_sel:[1,0]
	v_pk_mul_f32 v[8:9], v[138:139], v[12:13]
	v_pk_fma_f32 v[12:13], v[2:3], v[18:19], v[10:11] neg_lo:[0,0,1] neg_hi:[0,0,1]
	v_pk_fma_f32 v[2:3], v[2:3], v[18:19], v[10:11] op_sel_hi:[0,1,1]
	v_mov_b32_e32 v2, v5
	v_mov_b32_e32 v13, v3
	v_pk_mul_f32 v[2:3], v[2:3], v[16:17] op_sel_hi:[0,1]
	v_pk_mul_f32 v[10:11], v[138:139], v[12:13]
	v_pk_fma_f32 v[12:13], v[4:5], v[20:21], v[2:3] neg_lo:[0,0,1] neg_hi:[0,0,1]
	v_pk_fma_f32 v[2:3], v[4:5], v[20:21], v[2:3] op_sel_hi:[0,1,1]
	v_mov_b32_e32 v13, v3
	v_pk_mul_f32 v[12:13], v[138:139], v[12:13]
	v_cvt_pk_f16_f32 v2, v6, v7
	v_cvt_pk_f16_f32 v3, v8, v9
	v_cvt_pk_f16_f32 v4, v10, v11
	v_cvt_pk_f16_f32 v5, v12, v13
	s_mov_b64 s[0:1], -1
	s_cbranch_vccnz .LBB1_205
	s_mov_b64 s[0:1], 0
	v_mov_b64_e32 v[160:161], v[2:3]
	v_mov_b64_e32 v[162:163], v[4:5]
.LBB1_205:
	s_andn2_b64 vcc, exec, s[0:1]
	s_cbranch_vccnz .LBB1_207
	s_lshr_b32 s0, s20, 6
	v_or_b32_e32 v6, s0, v81
	v_lshlrev_b32_e32 v6, 5, v6
	v_or3_b32 v6, v80, v6, 64
	v_ashrrev_i32_e32 v7, 31, v6
	v_lshlrev_b64 v[6:7], 13, v[6:7]
	v_lshl_add_u64 v[6:7], v[14:15], 0, v[6:7]
	v_mov_b64_e32 v[160:161], v[2:3]
	v_mov_b64_e32 v[162:163], v[4:5]

.LBB1_222:
	s_waitcnt lgkmcnt(0)
	s_cmp_gt_u32 s54, 15
	s_cbranch_scc1 .Lqs_done
	s_cmp_lt_u32 s54, 8
	s_cbranch_scc0 .Lqs_8_16
	s_cmp_lt_u32 s54, 4
	s_cbranch_scc0 .Lqs_4_8
	s_cmp_lt_u32 s54, 2
	s_cbranch_scc0 .Lqs_2_4
	s_cmp_lt_u32 s54, 1
	s_cbranch_scc0 .Lqs_1_2
	global_store_dwordx4 v[166:167], v[180:183], off
	s_branch .Lqs_done
.Lqs_1_2:
	global_store_dwordx4 v[166:167], v[184:187], off
	s_branch .Lqs_done
.Lqs_2_4:
	s_cmp_lt_u32 s54, 3
	s_cbranch_scc0 .Lqs_3_4
	global_store_dwordx4 v[166:167], v[188:191], off
	s_branch .Lqs_done
.Lqs_3_4:
	global_store_dwordx4 v[166:167], v[192:195], off
	s_branch .Lqs_done
.Lqs_4_8:
	s_cmp_lt_u32 s54, 6
	s_cbranch_scc0 .Lqs_6_8
	s_cmp_lt_u32 s54, 5
	s_cbranch_scc0 .Lqs_5_6
	global_store_dwordx4 v[166:167], v[196:199], off
	s_branch .Lqs_done
.Lqs_5_6:
	global_store_dwordx4 v[166:167], v[200:203], off
	s_branch .Lqs_done
.Lqs_6_8:
	s_cmp_lt_u32 s54, 7
	s_cbranch_scc0 .Lqs_7_8
	global_store_dwordx4 v[166:167], v[204:207], off
	s_branch .Lqs_done
.Lqs_7_8:
	global_store_dwordx4 v[166:167], v[208:211], off
	s_branch .Lqs_done
.Lqs_8_16:
	s_cmp_lt_u32 s54, 12
	s_cbranch_scc0 .Lqs_12_16
	s_cmp_lt_u32 s54, 10
	s_cbranch_scc0 .Lqs_10_12
	s_cmp_lt_u32 s54, 9
	s_cbranch_scc0 .Lqs_9_10
	global_store_dwordx4 v[166:167], v[212:215], off
	s_branch .Lqs_done
.Lqs_9_10:
	global_store_dwordx4 v[166:167], v[216:219], off
	s_branch .Lqs_done
.Lqs_10_12:
	s_cmp_lt_u32 s54, 11
	s_cbranch_scc0 .Lqs_11_12
	global_store_dwordx4 v[166:167], v[220:223], off
	s_branch .Lqs_done
.Lqs_11_12:
	global_store_dwordx4 v[166:167], v[224:227], off
	s_branch .Lqs_done
.Lqs_12_16:
	s_cmp_lt_u32 s54, 14
	s_cbranch_scc0 .Lqs_14_16
	s_cmp_lt_u32 s54, 13
	s_cbranch_scc0 .Lqs_13_14
	global_store_dwordx4 v[166:167], v[228:231], off
	s_branch .Lqs_done
.Lqs_13_14:
	global_store_dwordx4 v[166:167], v[232:235], off
	s_branch .Lqs_done
.Lqs_14_16:
	s_cmp_lt_u32 s54, 15
	s_cbranch_scc0 .Lqs_15_16
	global_store_dwordx4 v[166:167], v[236:239], off
	s_branch .Lqs_done
.Lqs_15_16:
	global_store_dwordx4 v[166:167], v[160:163], off
	s_branch .Lqs_done
.Lqs_done:
	s_barrier
	s_setprio 1
	s_waitcnt lgkmcnt(0)
	v_mfma_f32_16x16x32_f16 v[60:63], v[112:115], v[104:107], v[60:63]
	s_add_i32 s89, s54, 1
	v_mfma_f32_16x16x32_f16 v[56:59], v[120:123], v[104:107], v[56:59]
	s_lshr_b32 s90, s89, 3
	v_mfma_f32_16x16x32_f16 v[44:47], v[112:115], v[80:83], v[44:47]
	s_mul_i32 s90, s90, s86
	v_mfma_f32_16x16x32_f16 v[40:43], v[120:123], v[80:83], v[40:43]
	s_bfe_u32 s92, s89, 0x20001
	v_mfma_f32_16x16x32_f16 v[28:31], v[112:115], v[72:75], v[28:31]
	s_mul_i32 s92, s92, s87
	v_mfma_f32_16x16x32_f16 v[24:27], v[120:123], v[72:75], v[24:27]
	s_add_u32 s90, s90, s92
	v_mfma_f32_16x16x32_f16 v[12:15], v[112:115], v[64:67], v[12:15]
	s_and_b32 s92, s89, 1
	v_mfma_f32_16x16x32_f16 v[8:11], v[120:123], v[64:67], v[8:11]
	s_mul_i32 s92, s92, s88
	v_mfma_f32_16x16x32_f16 v[60:63], v[116:119], v[108:111], v[60:63]
	s_add_u32 s90, s90, s92
	v_mfma_f32_16x16x32_f16 v[56:59], v[124:127], v[108:111], v[56:59]
	s_mov_b32 s91, 0
	v_mfma_f32_16x16x32_f16 v[44:47], v[116:119], v[84:87], v[44:47]
	v_lshl_add_u64 v[166:167], v[164:165], 0, s[90:91]
	v_mfma_f32_16x16x32_f16 v[40:43], v[124:127], v[84:87], v[40:43]
	v_mfma_f32_16x16x32_f16 v[28:31], v[116:119], v[76:79], v[28:31]
	v_mfma_f32_16x16x32_f16 v[24:27], v[124:127], v[76:79], v[24:27]
	v_mfma_f32_16x16x32_f16 v[12:15], v[116:119], v[68:71], v[12:15]
	v_mfma_f32_16x16x32_f16 v[8:11], v[124:127], v[68:71], v[8:11]
	s_setprio 0
	s_setprio 1
	v_mfma_f32_16x16x32_f16 v[52:55], v[88:91], v[104:107], v[52:55]
	v_mfma_f32_16x16x32_f16 v[48:51], v[96:99], v[104:107], v[48:51]
	v_mfma_f32_16x16x32_f16 v[36:39], v[88:91], v[80:83], v[36:39]
	v_mfma_f32_16x16x32_f16 v[32:35], v[96:99], v[80:83], v[32:35]
	v_mfma_f32_16x16x32_f16 v[20:23], v[88:91], v[72:75], v[20:23]
	v_mfma_f32_16x16x32_f16 v[16:19], v[96:99], v[72:75], v[16:19]
	v_mfma_f32_16x16x32_f16 v[4:7], v[88:91], v[64:67], v[4:7]
	v_mfma_f32_16x16x32_f16 v[0:3], v[96:99], v[64:67], v[0:3]
	v_mfma_f32_16x16x32_f16 v[52:55], v[92:95], v[108:111], v[52:55]
	v_mfma_f32_16x16x32_f16 v[48:51], v[100:103], v[108:111], v[48:51]
	v_mfma_f32_16x16x32_f16 v[36:39], v[92:95], v[84:87], v[36:39]
	v_mfma_f32_16x16x32_f16 v[32:35], v[100:103], v[84:87], v[32:35]
	v_mfma_f32_16x16x32_f16 v[20:23], v[92:95], v[76:79], v[20:23]
	v_mfma_f32_16x16x32_f16 v[16:19], v[100:103], v[76:79], v[16:19]
	v_mfma_f32_16x16x32_f16 v[4:7], v[92:95], v[68:71], v[4:7]
	v_mfma_f32_16x16x32_f16 v[0:3], v[100:103], v[68:71], v[0:3]
	s_setprio 0
	s_barrier
	s_add_i32 s20, s48, 0xc000
	s_cmp_lg_u32 s48, 0x18000
	s_cselect_b32 s20, s20, 0
	s_add_i32 s54, s54, 1
	s_mov_b32 s51, s48
	s_mov_b32 s48, s20
	s_cmp_eq_u32 s46, s54
	s_cbranch_scc1 .LBB1_234

	.amdhsa_kernel _Z10qkv_kernelN3pg84GemmENS_7EpiRopeEN2hg4GemmENS2_7EpiRopeE
		.amdhsa_group_segment_fixed_size 0
		.amdhsa_private_segment_fixed_size 0
		.amdhsa_kernarg_size 368
		.amdhsa_user_sgpr_count 2
		.amdhsa_user_sgpr_dispatch_ptr 0
		.amdhsa_user_sgpr_queue_ptr 0
		.amdhsa_user_sgpr_kernarg_segment_ptr 1
		.amdhsa_user_sgpr_dispatch_id 0
		.amdhsa_user_sgpr_kernarg_preload_length 0
		.amdhsa_user_sgpr_kernarg_preload_offset 0
		.amdhsa_user_sgpr_private_segment_size 0
		.amdhsa_uses_dynamic_stack 0
		.amdhsa_enable_private_segment 0
		.amdhsa_system_sgpr_workgroup_id_x 1
		.amdhsa_system_sgpr_workgroup_id_y 0
		.amdhsa_system_sgpr_workgroup_id_z 0
		.amdhsa_system_sgpr_workgroup_info 0
		.amdhsa_system_vgpr_workitem_id 0
		.amdhsa_next_free_vgpr 240
		.amdhsa_next_free_sgpr 93
		.amdhsa_accum_offset 240
		.amdhsa_reserve_vcc 1
		.amdhsa_float_round_mode_32 0
		.amdhsa_float_round_mode_16_64 0
		.amdhsa_float_denorm_mode_32 3
		.amdhsa_float_denorm_mode_16_64 3
		.amdhsa_dx10_clamp 1
		.amdhsa_ieee_mode 1
		.amdhsa_fp16_overflow 0
		.amdhsa_tg_split 0
		.amdhsa_exception_fp_ieee_invalid_op 0
		.amdhsa_exception_fp_denorm_src 0
		.amdhsa_exception_fp_ieee_div_zero 0
		.amdhsa_exception_fp_ieee_overflow 0
		.amdhsa_exception_fp_ieee_underflow 0
		.amdhsa_exception_fp_ieee_inexact 0
		.amdhsa_exception_int_div_zero 0
	.end_amdhsa_kernel

amdhsa.kernels:
  - .agpr_count:     0
    .args:
      - .actual_access:  read_only
        .address_space:  global
        .offset:         0
        .size:           8
        .value_kind:     global_buffer
      - .actual_access:  read_only
        .address_space:  global
        .offset:         8
        .size:           8
        .value_kind:     global_buffer
      - .actual_access:  read_only
        .address_space:  global
        .offset:         16
        .size:           8
        .value_kind:     global_buffer
      - .actual_access:  read_only
        .address_space:  global
        .offset:         24
        .size:           8
        .value_kind:     global_buffer
      - .actual_access:  read_only
        .address_space:  global
        .offset:         32
        .size:           8
        .value_kind:     global_buffer
      - .actual_access:  read_only
        .address_space:  global
        .offset:         40
        .size:           8
        .value_kind:     global_buffer
      - .address_space:  global
        .offset:         48
        .size:           8
        .value_kind:     global_buffer
      - .address_space:  global
        .offset:         56
        .size:           8
        .value_kind:     global_buffer
      - .address_space:  global
        .offset:         64
        .size:           8
        .value_kind:     global_buffer
      - .address_space:  global
        .offset:         72
        .size:           8
        .value_kind:     global_buffer
    .group_segment_fixed_size: 0
    .kernarg_segment_align: 8
    .kernarg_segment_size: 80
    .language:       OpenCL C
    .language_version:
      - 2
      - 0
    .max_flat_workgroup_size: 256
    .name:           _Z11prep_kernelPKfPKiS0_S0_S0_S0_PtS3_S3_P15HIP_vector_typeIfLj2EE
    .private_segment_fixed_size: 0
    .sgpr_count:     40
    .sgpr_spill_count: 0
    .symbol:         _Z11prep_kernelPKfPKiS0_S0_S0_S0_PtS3_S3_P15HIP_vector_typeIfLj2EE.kd
    .uniform_work_group_size: 1
    .uses_dynamic_stack: false
    .vgpr_count:     40
    .vgpr_spill_count: 0
    .wavefront_size: 64
  - .agpr_count:     0
    .args:
      - .offset:         0
        .size:           32
        .value_kind:     by_value
      - .offset:         32
        .size:           24
        .value_kind:     by_value
      - .offset:         56
        .size:           32
        .value_kind:     by_value
      - .offset:         88
        .size:           24
        .value_kind:     by_value
      - .offset:         112
        .size:           4
        .value_kind:     hidden_block_count_x
      - .offset:         116
        .size:           4
        .value_kind:     hidden_block_count_y
      - .offset:         120
        .size:           4
        .value_kind:     hidden_block_count_z
      - .offset:         124
        .size:           2
        .value_kind:     hidden_group_size_x
      - .offset:         126
        .size:           2
        .value_kind:     hidden_group_size_y
      - .offset:         128
        .size:           2
        .value_kind:     hidden_group_size_z
      - .offset:         130
        .size:           2
        .value_kind:     hidden_remainder_x
      - .offset:         132
        .size:           2
        .value_kind:     hidden_remainder_y
      - .offset:         134
        .size:           2
        .value_kind:     hidden_remainder_z
      - .offset:         152
        .size:           8
        .value_kind:     hidden_global_offset_x
      - .offset:         160
        .size:           8
        .value_kind:     hidden_global_offset_y
      - .offset:         168
        .size:           8
        .value_kind:     hidden_global_offset_z
      - .offset:         176
        .size:           2
        .value_kind:     hidden_grid_dims
      - .offset:         232
        .size:           4
        .value_kind:     hidden_dynamic_lds_size
    .group_segment_fixed_size: 0
    .kernarg_segment_align: 8
    .kernarg_segment_size: 368
    .language:       OpenCL C
    .language_version:
      - 2
      - 0
    .max_flat_workgroup_size: 512
    .name:           _Z10qkv_kernelN3pg84GemmENS_7EpiRopeEN2hg4GemmENS2_7EpiRopeE
    .private_segment_fixed_size: 0
    .sgpr_count:     99
    .sgpr_spill_count: 0
    .symbol:         _Z10qkv_kernelN3pg84GemmENS_7EpiRopeEN2hg4GemmENS2_7EpiRopeE.kd
    .uniform_work_group_size: 1
    .uses_dynamic_stack: false
    .vgpr_count:     240
    .vgpr_spill_count: 0
    .wavefront_size: 64
  - .agpr_count:     0
    .args:
      - .address_space:  global
        .offset:         0
        .size:           8
        .value_kind:     global_buffer
      - .address_space:  global
        .offset:         8
        .size:           8
        .value_kind:     global_buffer
      - .address_space:  global
        .offset:         16
        .size:           8
        .value_kind:     global_buffer
      - .address_space:  global
        .offset:         24
        .size:           8
        .value_kind:     global_buffer
    .group_segment_fixed_size: 0
    .kernarg_segment_align: 8
    .kernarg_segment_size: 32
    .language:       OpenCL C
    .language_version:
      - 2
      - 0
    .max_flat_workgroup_size: 512
    .name:           _Z11attn_kernelPKDF16_S0_S0_PDF16_
    .private_segment_fixed_size: 0
    .sgpr_count:     56
    .sgpr_spill_count: 0
    .symbol:         _Z11attn_kernelPKDF16_S0_S0_PDF16_.kd
    .uniform_work_group_size: 1
    .uses_dynamic_stack: false
    .vgpr_count:     243
    .vgpr_spill_count: 0
    .wavefront_size: 64
  - .agpr_count:     0
    .args:
      - .offset:         0
        .size:           32
        .value_kind:     by_value
      - .offset:         32
        .size:           16
        .value_kind:     by_value
      - .offset:         48
        .size:           4
        .value_kind:     hidden_block_count_x
      - .offset:         52
        .size:           4
        .value_kind:     hidden_block_count_y
      - .offset:         56
        .size:           4
        .value_kind:     hidden_block_count_z
      - .offset:         60
        .size:           2
        .value_kind:     hidden_group_size_x
      - .offset:         62
        .size:           2
        .value_kind:     hidden_group_size_y
      - .offset:         64
        .size:           2
        .value_kind:     hidden_group_size_z
      - .offset:         66
        .size:           2
        .value_kind:     hidden_remainder_x
      - .offset:         68
        .size:           2
        .value_kind:     hidden_remainder_y
      - .offset:         70
        .size:           2
        .value_kind:     hidden_remainder_z
      - .offset:         88
        .size:           8
        .value_kind:     hidden_global_offset_x
      - .offset:         96
        .size:           8
        .value_kind:     hidden_global_offset_y
      - .offset:         104
        .size:           8
        .value_kind:     hidden_global_offset_z
      - .offset:         112
        .size:           2
        .value_kind:     hidden_grid_dims
      - .offset:         168
        .size:           4
        .value_kind:     hidden_dynamic_lds_size
    .group_segment_fixed_size: 0
    .kernarg_segment_align: 8
    .kernarg_segment_size: 304
    .language:       OpenCL C
    .language_version:
      - 2
      - 0
    .max_flat_workgroup_size: 512
    .name:           _Z12hgemm_kernelIN2hg6EpiF32EEvNS0_4GemmET_
    .private_segment_fixed_size: 0
    .sgpr_count:     62
    .sgpr_spill_count: 0
    .symbol:         _Z12hgemm_kernelIN2hg6EpiF32EEvNS0_4GemmET_.kd
    .uniform_work_group_size: 1
    .uses_dynamic_stack: false
    .vgpr_count:     138
    .vgpr_spill_count: 0
    .wavefront_size: 64
